# adds nt hint on the merge-gate (sigmoid) stores of the w_in GEMM epilogue, which are not read again until the merge GEMM three phases later
# speedup vs baseline: 1.0185x; 1.0027x over previous
.LBB0_343:
	s_andn2_b64 vcc, exec, s[6:7]
	s_cbranch_vccnz .LBB0_345
	v_mul_f32_e32 v2, 0xbfb8aa3b, v128
	v_exp_f32_e32 v2, v2
	s_ashr_i32 s77, s76, 31
	v_add_f32_e32 v2, 1.0, v2
	v_rcp_f32_e32 v2, v2
	v_mul_f32_e32 v132, 0xbfb8aa3b, v124
	v_exp_f32_e32 v132, v132
	s_nop 0
	v_add_f32_e32 v132, 1.0, v132
	v_rcp_f32_e32 v134, v132
	v_mul_f32_e32 v132, 0xbfb8aa3b, v129
	v_exp_f32_e32 v132, v132
	s_nop 0
	v_add_f32_e32 v132, 1.0, v132
	v_rcp_f32_e32 v132, v132
	v_mul_f32_e32 v133, 0xbfb8aa3b, v125
	v_exp_f32_e32 v133, v133
	v_cvt_pk_bf16_f32 v132, v2, v132
	s_nop 0
	v_add_f32_e32 v133, 1.0, v133
	v_rcp_f32_e32 v135, v133
	v_mul_f32_e32 v133, 0xbfb8aa3b, v130
	v_exp_f32_e32 v133, v133
	s_nop 0
	v_add_f32_e32 v133, 1.0, v133
	v_rcp_f32_e32 v133, v133
	v_mul_f32_e32 v136, 0xbfb8aa3b, v126
	v_exp_f32_e32 v136, v136
	s_nop 0
	v_add_f32_e32 v136, 1.0, v136
	v_rcp_f32_e32 v136, v136
	v_mul_f32_e32 v137, 0xbfb8aa3b, v131
	v_exp_f32_e32 v137, v137
	s_nop 0
	v_add_f32_e32 v137, 1.0, v137
	v_rcp_f32_e32 v137, v137
	v_mul_f32_e32 v138, 0xbfb8aa3b, v127
	v_exp_f32_e32 v138, v138
	v_cvt_pk_bf16_f32 v133, v133, v137
	v_cvt_pk_bf16_f32 v134, v134, v135
	s_nop 0
	v_add_f32_e32 v138, 1.0, v138
	s_lshl_b64 s[6:7], s[76:77], 10
	v_rcp_f32_e32 v138, v138
	s_nop 0
	v_cvt_pk_bf16_f32 v135, v136, v138
	v_lshl_add_u64 v[136:137], v[148:149], 0, s[6:7]
	global_store_dwordx4 v[136:137], v[132:135], off nt

.LBB0_355:
	v_cndmask_b32_e64 v2, 0, 1, s[0:1]
	v_cmp_ne_u32_e64 s[42:43], 1, v2
	v_cndmask_b32_e64 v2, 0, 1, s[2:3]
	v_or_b32_e32 v132, s59, v165
	s_mov_b64 s[4:5], -1
	s_andn2_b64 vcc, exec, s[0:1]
	v_cmp_ne_u32_e64 s[40:41], 1, v2
	s_cbranch_vccnz .LBB0_363
	s_and_b64 vcc, exec, s[40:41]
	s_mov_b64 s[0:1], -1
	s_cbranch_vccnz .LBB0_360
	s_andn2_b64 vcc, exec, s[36:37]
	s_cbranch_vccnz .LBB0_359
	v_mul_f32_e32 v2, 0xbfb8aa3b, v120
	v_exp_f32_e32 v2, v2
	s_nop 0
	v_add_f32_e32 v2, 1.0, v2
	v_rcp_f32_e32 v2, v2
	v_mul_f32_e32 v124, 0xbfb8aa3b, v116
	v_exp_f32_e32 v124, v124
	s_nop 0
	v_add_f32_e32 v124, 1.0, v124
	v_rcp_f32_e32 v126, v124
	v_mul_f32_e32 v124, 0xbfb8aa3b, v121
	v_exp_f32_e32 v124, v124
	s_nop 0
	v_add_f32_e32 v124, 1.0, v124
	v_rcp_f32_e32 v124, v124
	v_mul_f32_e32 v125, 0xbfb8aa3b, v117
	v_exp_f32_e32 v125, v125
	v_cvt_pk_bf16_f32 v124, v2, v124
	s_nop 0
	v_add_f32_e32 v125, 1.0, v125
	v_rcp_f32_e32 v127, v125
	v_mul_f32_e32 v125, 0xbfb8aa3b, v122
	v_exp_f32_e32 v125, v125
	s_nop 0
	v_add_f32_e32 v125, 1.0, v125
	v_rcp_f32_e32 v125, v125
	v_mul_f32_e32 v128, 0xbfb8aa3b, v118
	v_exp_f32_e32 v128, v128
	s_nop 0
	v_add_f32_e32 v128, 1.0, v128
	v_rcp_f32_e32 v128, v128
	v_mul_f32_e32 v129, 0xbfb8aa3b, v123
	v_exp_f32_e32 v129, v129
	s_nop 0
	v_add_f32_e32 v129, 1.0, v129
	v_rcp_f32_e32 v129, v129
	v_mul_f32_e32 v130, 0xbfb8aa3b, v119
	v_exp_f32_e32 v130, v130
	v_cvt_pk_bf16_f32 v125, v125, v129
	v_cvt_pk_bf16_f32 v126, v126, v127
	s_nop 0
	v_add_f32_e32 v130, 1.0, v130
	s_or_b32 s0, s76, 4
	s_ashr_i32 s1, s0, 31
	s_lshl_b64 s[0:1], s[0:1], 10
	v_rcp_f32_e32 v130, v130
	s_nop 0
	v_cvt_pk_bf16_f32 v127, v128, v130
	v_lshl_add_u64 v[128:129], v[148:149], 0, s[0:1]
	global_store_dwordx4 v[128:129], v[124:127], off nt

.LBB0_379:
	s_andn2_b64 vcc, exec, s[0:1]
	s_cbranch_vccnz .LBB0_381
	v_mul_f32_e32 v2, 0xbfb8aa3b, v112
	v_exp_f32_e32 v2, v2
	s_ashr_i32 s83, s82, 31
	v_add_f32_e32 v2, 1.0, v2
	v_rcp_f32_e32 v2, v2
	v_mul_f32_e32 v116, 0xbfb8aa3b, v108
	v_exp_f32_e32 v116, v116
	s_nop 0
	v_add_f32_e32 v116, 1.0, v116
	v_rcp_f32_e32 v118, v116
	v_mul_f32_e32 v116, 0xbfb8aa3b, v113
	v_exp_f32_e32 v116, v116
	s_nop 0
	v_add_f32_e32 v116, 1.0, v116
	v_rcp_f32_e32 v116, v116
	v_mul_f32_e32 v117, 0xbfb8aa3b, v109
	v_exp_f32_e32 v117, v117
	v_cvt_pk_bf16_f32 v116, v2, v116
	s_nop 0
	v_add_f32_e32 v117, 1.0, v117
	v_rcp_f32_e32 v119, v117
	v_mul_f32_e32 v117, 0xbfb8aa3b, v114
	v_exp_f32_e32 v117, v117
	s_nop 0
	v_add_f32_e32 v117, 1.0, v117
	v_rcp_f32_e32 v117, v117
	v_mul_f32_e32 v121, 0xbfb8aa3b, v110
	v_exp_f32_e32 v121, v121
	s_nop 0
	v_add_f32_e32 v121, 1.0, v121
	v_rcp_f32_e32 v121, v121
	v_mul_f32_e32 v122, 0xbfb8aa3b, v115
	v_exp_f32_e32 v122, v122
	s_nop 0
	v_add_f32_e32 v122, 1.0, v122
	v_rcp_f32_e32 v122, v122
	v_mul_f32_e32 v123, 0xbfb8aa3b, v111
	v_exp_f32_e32 v123, v123
	v_cvt_pk_bf16_f32 v117, v117, v122
	v_cvt_pk_bf16_f32 v118, v118, v119
	s_nop 0
	v_add_f32_e32 v123, 1.0, v123
	s_lshl_b64 s[0:1], s[82:83], 10
	s_movk_i32 s83, 0x2000
	v_rcp_f32_e32 v123, v123
	s_nop 0
	v_cvt_pk_bf16_f32 v119, v121, v123
	v_lshl_add_u64 v[122:123], v[148:149], 0, s[0:1]
	global_store_dwordx4 v[122:123], v[116:119], off nt

.LBB0_390:
	s_and_b64 vcc, exec, s[40:41]
	s_cbranch_vccnz .LBB0_394
	s_andn2_b64 vcc, exec, s[36:37]
	s_cbranch_vccnz .LBB0_393
	v_mul_f32_e32 v2, 0xbfb8aa3b, v104
	v_exp_f32_e32 v2, v2
	s_nop 0
	v_add_f32_e32 v2, 1.0, v2
	v_rcp_f32_e32 v2, v2
	v_mul_f32_e32 v108, 0xbfb8aa3b, v100
	v_exp_f32_e32 v108, v108
	s_nop 0
	v_add_f32_e32 v108, 1.0, v108
	v_rcp_f32_e32 v110, v108
	v_mul_f32_e32 v108, 0xbfb8aa3b, v105
	v_exp_f32_e32 v108, v108
	s_nop 0
	v_add_f32_e32 v108, 1.0, v108
	v_rcp_f32_e32 v108, v108
	v_mul_f32_e32 v109, 0xbfb8aa3b, v101
	v_exp_f32_e32 v109, v109
	v_cvt_pk_bf16_f32 v108, v2, v108
	s_nop 0
	v_add_f32_e32 v109, 1.0, v109
	v_rcp_f32_e32 v111, v109
	v_mul_f32_e32 v109, 0xbfb8aa3b, v106
	v_exp_f32_e32 v109, v109
	s_nop 0
	v_add_f32_e32 v109, 1.0, v109
	v_rcp_f32_e32 v109, v109
	v_mul_f32_e32 v112, 0xbfb8aa3b, v102
	v_exp_f32_e32 v112, v112
	s_nop 0
	v_add_f32_e32 v112, 1.0, v112
	v_rcp_f32_e32 v112, v112
	v_mul_f32_e32 v113, 0xbfb8aa3b, v107
	v_exp_f32_e32 v113, v113
	s_nop 0
	v_add_f32_e32 v113, 1.0, v113
	v_rcp_f32_e32 v113, v113
	v_mul_f32_e32 v114, 0xbfb8aa3b, v103
	v_exp_f32_e32 v114, v114
	v_cvt_pk_bf16_f32 v109, v109, v113
	v_cvt_pk_bf16_f32 v110, v110, v111
	s_nop 0
	v_add_f32_e32 v114, 1.0, v114
	s_or_b32 s0, s82, 4
	s_ashr_i32 s1, s0, 31
	s_lshl_b64 s[0:1], s[0:1], 10
	v_rcp_f32_e32 v114, v114
	s_nop 0
	v_cvt_pk_bf16_f32 v111, v112, v114
	v_lshl_add_u64 v[112:113], v[148:149], 0, s[0:1]
	global_store_dwordx4 v[112:113], v[108:111], off nt

.LBB0_411:
	s_andn2_b64 vcc, exec, s[0:1]
	s_cbranch_vccnz .LBB0_413
	v_mul_f32_e32 v2, 0xbfb8aa3b, v96
	v_exp_f32_e32 v2, v2
	s_ashr_i32 s83, s82, 31
	v_add_f32_e32 v2, 1.0, v2
	v_rcp_f32_e32 v2, v2
	v_mul_f32_e32 v100, 0xbfb8aa3b, v92
	v_exp_f32_e32 v100, v100
	s_nop 0
	v_add_f32_e32 v100, 1.0, v100
	v_rcp_f32_e32 v102, v100
	v_mul_f32_e32 v100, 0xbfb8aa3b, v97
	v_exp_f32_e32 v100, v100
	s_nop 0
	v_add_f32_e32 v100, 1.0, v100
	v_rcp_f32_e32 v100, v100
	v_mul_f32_e32 v101, 0xbfb8aa3b, v93
	v_exp_f32_e32 v101, v101
	v_cvt_pk_bf16_f32 v100, v2, v100
	s_nop 0
	v_add_f32_e32 v101, 1.0, v101
	v_rcp_f32_e32 v103, v101
	v_mul_f32_e32 v101, 0xbfb8aa3b, v98
	v_exp_f32_e32 v101, v101
	s_nop 0
	v_add_f32_e32 v101, 1.0, v101
	v_rcp_f32_e32 v101, v101
	v_mul_f32_e32 v105, 0xbfb8aa3b, v94
	v_exp_f32_e32 v105, v105
	s_nop 0
	v_add_f32_e32 v105, 1.0, v105
	v_rcp_f32_e32 v105, v105
	v_mul_f32_e32 v106, 0xbfb8aa3b, v99
	v_exp_f32_e32 v106, v106
	s_nop 0
	v_add_f32_e32 v106, 1.0, v106
	v_rcp_f32_e32 v106, v106
	v_mul_f32_e32 v107, 0xbfb8aa3b, v95
	v_exp_f32_e32 v107, v107
	v_cvt_pk_bf16_f32 v101, v101, v106
	v_cvt_pk_bf16_f32 v102, v102, v103
	s_nop 0
	v_add_f32_e32 v107, 1.0, v107
	s_lshl_b64 s[0:1], s[82:83], 10
	s_movk_i32 s83, 0x2000
	v_rcp_f32_e32 v107, v107
	s_nop 0
	v_cvt_pk_bf16_f32 v103, v105, v107
	v_lshl_add_u64 v[106:107], v[148:149], 0, s[0:1]
	global_store_dwordx4 v[106:107], v[100:103], off nt

.LBB0_422:
	s_and_b64 vcc, exec, s[40:41]
	s_cbranch_vccnz .LBB0_426
	s_andn2_b64 vcc, exec, s[36:37]
	s_cbranch_vccnz .LBB0_425
	v_mul_f32_e32 v2, 0xbfb8aa3b, v88
	v_exp_f32_e32 v2, v2
	s_nop 0
	v_add_f32_e32 v2, 1.0, v2
	v_rcp_f32_e32 v2, v2
	v_mul_f32_e32 v92, 0xbfb8aa3b, v84
	v_exp_f32_e32 v92, v92
	s_nop 0
	v_add_f32_e32 v92, 1.0, v92
	v_rcp_f32_e32 v94, v92
	v_mul_f32_e32 v92, 0xbfb8aa3b, v89
	v_exp_f32_e32 v92, v92
	s_nop 0
	v_add_f32_e32 v92, 1.0, v92
	v_rcp_f32_e32 v92, v92
	v_mul_f32_e32 v93, 0xbfb8aa3b, v85
	v_exp_f32_e32 v93, v93
	v_cvt_pk_bf16_f32 v92, v2, v92
	s_nop 0
	v_add_f32_e32 v93, 1.0, v93
	v_rcp_f32_e32 v95, v93
	v_mul_f32_e32 v93, 0xbfb8aa3b, v90
	v_exp_f32_e32 v93, v93
	s_nop 0
	v_add_f32_e32 v93, 1.0, v93
	v_rcp_f32_e32 v93, v93
	v_mul_f32_e32 v96, 0xbfb8aa3b, v86
	v_exp_f32_e32 v96, v96
	s_nop 0
	v_add_f32_e32 v96, 1.0, v96
	v_rcp_f32_e32 v96, v96
	v_mul_f32_e32 v97, 0xbfb8aa3b, v91
	v_exp_f32_e32 v97, v97
	s_nop 0
	v_add_f32_e32 v97, 1.0, v97
	v_rcp_f32_e32 v97, v97
	v_mul_f32_e32 v98, 0xbfb8aa3b, v87
	v_exp_f32_e32 v98, v98
	v_cvt_pk_bf16_f32 v93, v93, v97
	v_cvt_pk_bf16_f32 v94, v94, v95
	s_nop 0
	v_add_f32_e32 v98, 1.0, v98
	s_or_b32 s0, s82, 4
	s_ashr_i32 s1, s0, 31
	s_lshl_b64 s[0:1], s[0:1], 10
	v_rcp_f32_e32 v98, v98
	s_nop 0
	v_cvt_pk_bf16_f32 v95, v96, v98
	v_lshl_add_u64 v[96:97], v[148:149], 0, s[0:1]
	global_store_dwordx4 v[96:97], v[92:95], off nt

.LBB0_443:
	s_andn2_b64 vcc, exec, s[0:1]
	s_cbranch_vccnz .LBB0_445
	v_mul_f32_e32 v2, 0xbfb8aa3b, v80
	v_exp_f32_e32 v2, v2
	s_ashr_i32 s83, s82, 31
	v_add_f32_e32 v2, 1.0, v2
	v_rcp_f32_e32 v2, v2
	v_mul_f32_e32 v84, 0xbfb8aa3b, v76
	v_exp_f32_e32 v84, v84
	s_nop 0
	v_add_f32_e32 v84, 1.0, v84
	v_rcp_f32_e32 v86, v84
	v_mul_f32_e32 v84, 0xbfb8aa3b, v81
	v_exp_f32_e32 v84, v84
	s_nop 0
	v_add_f32_e32 v84, 1.0, v84
	v_rcp_f32_e32 v84, v84
	v_mul_f32_e32 v85, 0xbfb8aa3b, v77
	v_exp_f32_e32 v85, v85
	v_cvt_pk_bf16_f32 v84, v2, v84
	s_nop 0
	v_add_f32_e32 v85, 1.0, v85
	v_rcp_f32_e32 v87, v85
	v_mul_f32_e32 v85, 0xbfb8aa3b, v82
	v_exp_f32_e32 v85, v85
	s_nop 0
	v_add_f32_e32 v85, 1.0, v85
	v_rcp_f32_e32 v85, v85
	v_mul_f32_e32 v89, 0xbfb8aa3b, v78
	v_exp_f32_e32 v89, v89
	s_nop 0
	v_add_f32_e32 v89, 1.0, v89
	v_rcp_f32_e32 v89, v89
	v_mul_f32_e32 v90, 0xbfb8aa3b, v83
	v_exp_f32_e32 v90, v90
	s_nop 0
	v_add_f32_e32 v90, 1.0, v90
	v_rcp_f32_e32 v90, v90
	v_mul_f32_e32 v91, 0xbfb8aa3b, v79
	v_exp_f32_e32 v91, v91
	v_cvt_pk_bf16_f32 v85, v85, v90
	v_cvt_pk_bf16_f32 v86, v86, v87
	s_nop 0
	v_add_f32_e32 v91, 1.0, v91
	s_lshl_b64 s[0:1], s[82:83], 10
	s_movk_i32 s83, 0x2000
	v_rcp_f32_e32 v91, v91
	s_nop 0
	v_cvt_pk_bf16_f32 v87, v89, v91
	v_lshl_add_u64 v[90:91], v[148:149], 0, s[0:1]
	global_store_dwordx4 v[90:91], v[84:87], off nt

.LBB0_454:
	s_and_b64 vcc, exec, s[40:41]
	s_cbranch_vccnz .LBB0_458
	s_andn2_b64 vcc, exec, s[36:37]
	s_cbranch_vccnz .LBB0_457
	v_mul_f32_e32 v2, 0xbfb8aa3b, v72
	v_exp_f32_e32 v2, v2
	s_nop 0
	v_add_f32_e32 v2, 1.0, v2
	v_rcp_f32_e32 v2, v2
	v_mul_f32_e32 v76, 0xbfb8aa3b, v68
	v_exp_f32_e32 v76, v76
	s_nop 0
	v_add_f32_e32 v76, 1.0, v76
	v_rcp_f32_e32 v78, v76
	v_mul_f32_e32 v76, 0xbfb8aa3b, v73
	v_exp_f32_e32 v76, v76
	s_nop 0
	v_add_f32_e32 v76, 1.0, v76
	v_rcp_f32_e32 v76, v76
	v_mul_f32_e32 v77, 0xbfb8aa3b, v69
	v_exp_f32_e32 v77, v77
	v_cvt_pk_bf16_f32 v76, v2, v76
	s_nop 0
	v_add_f32_e32 v77, 1.0, v77
	v_rcp_f32_e32 v79, v77
	v_mul_f32_e32 v77, 0xbfb8aa3b, v74
	v_exp_f32_e32 v77, v77
	s_nop 0
	v_add_f32_e32 v77, 1.0, v77
	v_rcp_f32_e32 v77, v77
	v_mul_f32_e32 v80, 0xbfb8aa3b, v70
	v_exp_f32_e32 v80, v80
	s_nop 0
	v_add_f32_e32 v80, 1.0, v80
	v_rcp_f32_e32 v80, v80
	v_mul_f32_e32 v81, 0xbfb8aa3b, v75
	v_exp_f32_e32 v81, v81
	s_nop 0
	v_add_f32_e32 v81, 1.0, v81
	v_rcp_f32_e32 v81, v81
	v_mul_f32_e32 v82, 0xbfb8aa3b, v71
	v_exp_f32_e32 v82, v82
	v_cvt_pk_bf16_f32 v77, v77, v81
	v_cvt_pk_bf16_f32 v78, v78, v79
	s_nop 0
	v_add_f32_e32 v82, 1.0, v82
	s_or_b32 s0, s82, 4
	s_ashr_i32 s1, s0, 31
	s_lshl_b64 s[0:1], s[0:1], 10
	v_rcp_f32_e32 v82, v82
	s_nop 0
	v_cvt_pk_bf16_f32 v79, v80, v82
	v_lshl_add_u64 v[80:81], v[148:149], 0, s[0:1]
	global_store_dwordx4 v[80:81], v[76:79], off nt

.LBB0_472:
	s_andn2_b64 vcc, exec, s[0:1]
	s_cbranch_vccnz .LBB0_474
	v_mul_f32_e32 v2, 0xbfb8aa3b, v64
	v_exp_f32_e32 v2, v2
	s_ashr_i32 s83, s82, 31
	v_add_f32_e32 v2, 1.0, v2
	v_rcp_f32_e32 v2, v2
	v_mul_f32_e32 v68, 0xbfb8aa3b, v60
	v_exp_f32_e32 v68, v68
	s_nop 0
	v_add_f32_e32 v68, 1.0, v68
	v_rcp_f32_e32 v70, v68
	v_mul_f32_e32 v68, 0xbfb8aa3b, v65
	v_exp_f32_e32 v68, v68
	s_nop 0
	v_add_f32_e32 v68, 1.0, v68
	v_rcp_f32_e32 v68, v68
	v_mul_f32_e32 v69, 0xbfb8aa3b, v61
	v_exp_f32_e32 v69, v69
	v_cvt_pk_bf16_f32 v68, v2, v68
	s_nop 0
	v_add_f32_e32 v69, 1.0, v69
	v_rcp_f32_e32 v71, v69
	v_mul_f32_e32 v69, 0xbfb8aa3b, v66
	v_exp_f32_e32 v69, v69
	s_nop 0
	v_add_f32_e32 v69, 1.0, v69
	v_rcp_f32_e32 v69, v69
	v_mul_f32_e32 v72, 0xbfb8aa3b, v62
	v_exp_f32_e32 v72, v72
	s_nop 0
	v_add_f32_e32 v72, 1.0, v72
	v_rcp_f32_e32 v72, v72
	v_mul_f32_e32 v73, 0xbfb8aa3b, v67
	v_exp_f32_e32 v73, v73
	s_nop 0
	v_add_f32_e32 v73, 1.0, v73
	v_rcp_f32_e32 v73, v73
	v_mul_f32_e32 v74, 0xbfb8aa3b, v63
	v_exp_f32_e32 v74, v74
	v_cvt_pk_bf16_f32 v69, v69, v73
	v_cvt_pk_bf16_f32 v70, v70, v71
	s_nop 0
	v_add_f32_e32 v74, 1.0, v74
	s_lshl_b64 s[0:1], s[82:83], 10
	s_movk_i32 s83, 0x2000
	v_rcp_f32_e32 v74, v74
	s_nop 0
	v_cvt_pk_bf16_f32 v71, v72, v74
	v_lshl_add_u64 v[72:73], v[148:149], 0, s[0:1]
	global_store_dwordx4 v[72:73], v[68:71], off nt

.LBB0_486:
	s_and_b64 vcc, exec, s[40:41]
	s_cbranch_vccnz .LBB0_490
	s_andn2_b64 vcc, exec, s[36:37]
	s_cbranch_vccnz .LBB0_489
	v_mul_f32_e32 v2, 0xbfb8aa3b, v56
	v_exp_f32_e32 v2, v2
	s_nop 0
	v_add_f32_e32 v2, 1.0, v2
	v_rcp_f32_e32 v2, v2
	v_mul_f32_e32 v60, 0xbfb8aa3b, v52
	v_exp_f32_e32 v60, v60
	s_nop 0
	v_add_f32_e32 v60, 1.0, v60
	v_rcp_f32_e32 v62, v60
	v_mul_f32_e32 v60, 0xbfb8aa3b, v57
	v_exp_f32_e32 v60, v60
	s_nop 0
	v_add_f32_e32 v60, 1.0, v60
	v_rcp_f32_e32 v60, v60
	v_mul_f32_e32 v61, 0xbfb8aa3b, v53
	v_exp_f32_e32 v61, v61
	v_cvt_pk_bf16_f32 v60, v2, v60
	s_nop 0
	v_add_f32_e32 v61, 1.0, v61
	v_rcp_f32_e32 v63, v61
	v_mul_f32_e32 v61, 0xbfb8aa3b, v58
	v_exp_f32_e32 v61, v61
	s_nop 0
	v_add_f32_e32 v61, 1.0, v61
	v_rcp_f32_e32 v61, v61
	v_mul_f32_e32 v64, 0xbfb8aa3b, v54
	v_exp_f32_e32 v64, v64
	s_nop 0
	v_add_f32_e32 v64, 1.0, v64
	v_rcp_f32_e32 v64, v64
	v_mul_f32_e32 v65, 0xbfb8aa3b, v59
	v_exp_f32_e32 v65, v65
	s_nop 0
	v_add_f32_e32 v65, 1.0, v65
	v_rcp_f32_e32 v65, v65
	v_mul_f32_e32 v66, 0xbfb8aa3b, v55
	v_exp_f32_e32 v66, v66
	v_cvt_pk_bf16_f32 v61, v61, v65
	v_cvt_pk_bf16_f32 v62, v62, v63
	s_nop 0
	v_add_f32_e32 v66, 1.0, v66
	s_or_b32 s0, s82, 4
	s_ashr_i32 s1, s0, 31
	s_lshl_b64 s[0:1], s[0:1], 10
	v_rcp_f32_e32 v66, v66
	s_nop 0
	v_cvt_pk_bf16_f32 v63, v64, v66
	v_lshl_add_u64 v[64:65], v[148:149], 0, s[0:1]
	global_store_dwordx4 v[64:65], v[60:63], off nt

.LBB0_507:
	s_andn2_b64 vcc, exec, s[0:1]
	s_cbranch_vccnz .LBB0_509
	v_mul_f32_e32 v2, 0xbfb8aa3b, v48
	v_exp_f32_e32 v2, v2
	s_ashr_i32 s83, s82, 31
	v_add_f32_e32 v2, 1.0, v2
	v_rcp_f32_e32 v2, v2
	v_mul_f32_e32 v52, 0xbfb8aa3b, v44
	v_exp_f32_e32 v52, v52
	s_nop 0
	v_add_f32_e32 v52, 1.0, v52
	v_rcp_f32_e32 v54, v52
	v_mul_f32_e32 v52, 0xbfb8aa3b, v49
	v_exp_f32_e32 v52, v52
	s_nop 0
	v_add_f32_e32 v52, 1.0, v52
	v_rcp_f32_e32 v52, v52
	v_mul_f32_e32 v53, 0xbfb8aa3b, v45
	v_exp_f32_e32 v53, v53
	v_cvt_pk_bf16_f32 v52, v2, v52
	s_nop 0
	v_add_f32_e32 v53, 1.0, v53
	v_rcp_f32_e32 v55, v53
	v_mul_f32_e32 v53, 0xbfb8aa3b, v50
	v_exp_f32_e32 v53, v53
	s_nop 0
	v_add_f32_e32 v53, 1.0, v53
	v_rcp_f32_e32 v53, v53
	v_mul_f32_e32 v57, 0xbfb8aa3b, v46
	v_exp_f32_e32 v57, v57
	s_nop 0
	v_add_f32_e32 v57, 1.0, v57
	v_rcp_f32_e32 v57, v57
	v_mul_f32_e32 v58, 0xbfb8aa3b, v51
	v_exp_f32_e32 v58, v58
	s_nop 0
	v_add_f32_e32 v58, 1.0, v58
	v_rcp_f32_e32 v58, v58
	v_mul_f32_e32 v59, 0xbfb8aa3b, v47
	v_exp_f32_e32 v59, v59
	v_cvt_pk_bf16_f32 v53, v53, v58
	v_cvt_pk_bf16_f32 v54, v54, v55
	s_nop 0
	v_add_f32_e32 v59, 1.0, v59
	s_lshl_b64 s[0:1], s[82:83], 10
	s_movk_i32 s83, 0x2000
	v_rcp_f32_e32 v59, v59
	s_nop 0
	v_cvt_pk_bf16_f32 v55, v57, v59
	v_lshl_add_u64 v[58:59], v[148:149], 0, s[0:1]
	global_store_dwordx4 v[58:59], v[52:55], off nt

.LBB0_518:
	s_and_b64 vcc, exec, s[40:41]
	s_cbranch_vccnz .LBB0_522
	s_andn2_b64 vcc, exec, s[36:37]
	s_cbranch_vccnz .LBB0_521
	v_mul_f32_e32 v2, 0xbfb8aa3b, v40
	v_exp_f32_e32 v2, v2
	s_nop 0
	v_add_f32_e32 v2, 1.0, v2
	v_rcp_f32_e32 v2, v2
	v_mul_f32_e32 v44, 0xbfb8aa3b, v36
	v_exp_f32_e32 v44, v44
	s_nop 0
	v_add_f32_e32 v44, 1.0, v44
	v_rcp_f32_e32 v46, v44
	v_mul_f32_e32 v44, 0xbfb8aa3b, v41
	v_exp_f32_e32 v44, v44
	s_nop 0
	v_add_f32_e32 v44, 1.0, v44
	v_rcp_f32_e32 v44, v44
	v_mul_f32_e32 v45, 0xbfb8aa3b, v37
	v_exp_f32_e32 v45, v45
	v_cvt_pk_bf16_f32 v44, v2, v44
	s_nop 0
	v_add_f32_e32 v45, 1.0, v45
	v_rcp_f32_e32 v47, v45
	v_mul_f32_e32 v45, 0xbfb8aa3b, v42
	v_exp_f32_e32 v45, v45
	s_nop 0
	v_add_f32_e32 v45, 1.0, v45
	v_rcp_f32_e32 v45, v45
	v_mul_f32_e32 v48, 0xbfb8aa3b, v38
	v_exp_f32_e32 v48, v48
	s_nop 0
	v_add_f32_e32 v48, 1.0, v48
	v_rcp_f32_e32 v48, v48
	v_mul_f32_e32 v49, 0xbfb8aa3b, v43
	v_exp_f32_e32 v49, v49
	s_nop 0
	v_add_f32_e32 v49, 1.0, v49
	v_rcp_f32_e32 v49, v49
	v_mul_f32_e32 v50, 0xbfb8aa3b, v39
	v_exp_f32_e32 v50, v50
	v_cvt_pk_bf16_f32 v45, v45, v49
	v_cvt_pk_bf16_f32 v46, v46, v47
	s_nop 0
	v_add_f32_e32 v50, 1.0, v50
	s_or_b32 s0, s82, 4
	s_ashr_i32 s1, s0, 31
	s_lshl_b64 s[0:1], s[0:1], 10
	v_rcp_f32_e32 v50, v50
	s_nop 0
	v_cvt_pk_bf16_f32 v47, v48, v50
	v_lshl_add_u64 v[48:49], v[148:149], 0, s[0:1]
	global_store_dwordx4 v[48:49], v[44:47], off nt

.LBB0_539:
	s_andn2_b64 vcc, exec, s[0:1]
	s_cbranch_vccnz .LBB0_541
	v_mul_f32_e32 v2, 0xbfb8aa3b, v32
	v_exp_f32_e32 v2, v2
	s_ashr_i32 s83, s82, 31
	v_add_f32_e32 v2, 1.0, v2
	v_rcp_f32_e32 v2, v2
	v_mul_f32_e32 v36, 0xbfb8aa3b, v28
	v_exp_f32_e32 v36, v36
	s_nop 0
	v_add_f32_e32 v36, 1.0, v36
	v_rcp_f32_e32 v38, v36
	v_mul_f32_e32 v36, 0xbfb8aa3b, v33
	v_exp_f32_e32 v36, v36
	s_nop 0
	v_add_f32_e32 v36, 1.0, v36
	v_rcp_f32_e32 v36, v36
	v_mul_f32_e32 v37, 0xbfb8aa3b, v29
	v_exp_f32_e32 v37, v37
	v_cvt_pk_bf16_f32 v36, v2, v36
	s_nop 0
	v_add_f32_e32 v37, 1.0, v37
	v_rcp_f32_e32 v39, v37
	v_mul_f32_e32 v37, 0xbfb8aa3b, v34
	v_exp_f32_e32 v37, v37
	s_nop 0
	v_add_f32_e32 v37, 1.0, v37
	v_rcp_f32_e32 v37, v37
	v_mul_f32_e32 v41, 0xbfb8aa3b, v30
	v_exp_f32_e32 v41, v41
	s_nop 0
	v_add_f32_e32 v41, 1.0, v41
	v_rcp_f32_e32 v41, v41
	v_mul_f32_e32 v42, 0xbfb8aa3b, v35
	v_exp_f32_e32 v42, v42
	s_nop 0
	v_add_f32_e32 v42, 1.0, v42
	v_rcp_f32_e32 v42, v42
	v_mul_f32_e32 v43, 0xbfb8aa3b, v31
	v_exp_f32_e32 v43, v43
	v_cvt_pk_bf16_f32 v37, v37, v42
	v_cvt_pk_bf16_f32 v38, v38, v39
	s_nop 0
	v_add_f32_e32 v43, 1.0, v43
	s_lshl_b64 s[0:1], s[82:83], 10
	s_movk_i32 s83, 0x2000
	v_rcp_f32_e32 v43, v43
	s_nop 0
	v_cvt_pk_bf16_f32 v39, v41, v43
	v_lshl_add_u64 v[42:43], v[148:149], 0, s[0:1]
	global_store_dwordx4 v[42:43], v[36:39], off nt

.LBB0_550:
	s_and_b64 vcc, exec, s[40:41]
	s_cbranch_vccnz .LBB0_554
	s_andn2_b64 vcc, exec, s[36:37]
	s_cbranch_vccnz .LBB0_553
	v_mul_f32_e32 v2, 0xbfb8aa3b, v24
	v_exp_f32_e32 v2, v2
	s_nop 0
	v_add_f32_e32 v2, 1.0, v2
	v_rcp_f32_e32 v2, v2
	v_mul_f32_e32 v28, 0xbfb8aa3b, v20
	v_exp_f32_e32 v28, v28
	s_nop 0
	v_add_f32_e32 v28, 1.0, v28
	v_rcp_f32_e32 v30, v28
	v_mul_f32_e32 v28, 0xbfb8aa3b, v25
	v_exp_f32_e32 v28, v28
	s_nop 0
	v_add_f32_e32 v28, 1.0, v28
	v_rcp_f32_e32 v28, v28
	v_mul_f32_e32 v29, 0xbfb8aa3b, v21
	v_exp_f32_e32 v29, v29
	v_cvt_pk_bf16_f32 v28, v2, v28
	s_nop 0
	v_add_f32_e32 v29, 1.0, v29
	v_rcp_f32_e32 v31, v29
	v_mul_f32_e32 v29, 0xbfb8aa3b, v26
	v_exp_f32_e32 v29, v29
	s_nop 0
	v_add_f32_e32 v29, 1.0, v29
	v_rcp_f32_e32 v29, v29
	v_mul_f32_e32 v32, 0xbfb8aa3b, v22
	v_exp_f32_e32 v32, v32
	s_nop 0
	v_add_f32_e32 v32, 1.0, v32
	v_rcp_f32_e32 v32, v32
	v_mul_f32_e32 v33, 0xbfb8aa3b, v27
	v_exp_f32_e32 v33, v33
	s_nop 0
	v_add_f32_e32 v33, 1.0, v33
	v_rcp_f32_e32 v33, v33
	v_mul_f32_e32 v34, 0xbfb8aa3b, v23
	v_exp_f32_e32 v34, v34
	v_cvt_pk_bf16_f32 v29, v29, v33
	v_cvt_pk_bf16_f32 v30, v30, v31
	s_nop 0
	v_add_f32_e32 v34, 1.0, v34
	s_or_b32 s0, s82, 4
	s_ashr_i32 s1, s0, 31
	s_lshl_b64 s[0:1], s[0:1], 10
	v_rcp_f32_e32 v34, v34
	s_nop 0
	v_cvt_pk_bf16_f32 v31, v32, v34
	v_lshl_add_u64 v[32:33], v[148:149], 0, s[0:1]
	global_store_dwordx4 v[32:33], v[28:31], off nt

.LBB0_572:
	s_andn2_b64 vcc, exec, s[0:1]
	s_cbranch_vccnz .LBB0_574
	v_mul_f32_e32 v2, 0xbfb8aa3b, v16
	v_exp_f32_e32 v2, v2
	s_ashr_i32 s77, s76, 31
	v_add_f32_e32 v2, 1.0, v2
	v_rcp_f32_e32 v2, v2
	v_mul_f32_e32 v20, 0xbfb8aa3b, v12
	v_exp_f32_e32 v20, v20
	s_nop 0
	v_add_f32_e32 v20, 1.0, v20
	v_rcp_f32_e32 v22, v20
	v_mul_f32_e32 v20, 0xbfb8aa3b, v17
	v_exp_f32_e32 v20, v20
	s_nop 0
	v_add_f32_e32 v20, 1.0, v20
	v_rcp_f32_e32 v20, v20
	v_mul_f32_e32 v21, 0xbfb8aa3b, v13
	v_exp_f32_e32 v21, v21
	v_cvt_pk_bf16_f32 v20, v2, v20
	s_nop 0
	v_add_f32_e32 v21, 1.0, v21
	v_rcp_f32_e32 v23, v21
	v_mul_f32_e32 v21, 0xbfb8aa3b, v18
	v_exp_f32_e32 v21, v21
	s_nop 0
	v_add_f32_e32 v21, 1.0, v21
	v_rcp_f32_e32 v21, v21
	v_mul_f32_e32 v25, 0xbfb8aa3b, v14
	v_exp_f32_e32 v25, v25
	s_nop 0
	v_add_f32_e32 v25, 1.0, v25
	v_rcp_f32_e32 v25, v25
	v_mul_f32_e32 v26, 0xbfb8aa3b, v19
	v_exp_f32_e32 v26, v26
	s_nop 0
	v_add_f32_e32 v26, 1.0, v26
	v_rcp_f32_e32 v26, v26
	v_mul_f32_e32 v27, 0xbfb8aa3b, v15
	v_exp_f32_e32 v27, v27
	v_cvt_pk_bf16_f32 v21, v21, v26
	v_cvt_pk_bf16_f32 v22, v22, v23
	s_nop 0
	v_add_f32_e32 v27, 1.0, v27
	s_lshl_b64 s[0:1], s[76:77], 10
	s_movk_i32 s77, 0x6000
	v_rcp_f32_e32 v27, v27
	s_nop 0
	v_cvt_pk_bf16_f32 v23, v25, v27
	v_lshl_add_u64 v[26:27], v[148:149], 0, s[0:1]
	global_store_dwordx4 v[26:27], v[20:23], off nt

.LBB0_583:
	s_and_b64 vcc, exec, s[40:41]
	s_cbranch_vccnz .LBB0_587
	s_andn2_b64 vcc, exec, s[36:37]
	s_cbranch_vccnz .LBB0_586
	v_mul_f32_e32 v2, 0xbfb8aa3b, v8
	v_exp_f32_e32 v2, v2
	s_nop 0
	v_add_f32_e32 v2, 1.0, v2
	v_rcp_f32_e32 v2, v2
	v_mul_f32_e32 v12, 0xbfb8aa3b, v4
	v_exp_f32_e32 v12, v12
	s_nop 0
	v_add_f32_e32 v12, 1.0, v12
	v_rcp_f32_e32 v14, v12
	v_mul_f32_e32 v12, 0xbfb8aa3b, v9
	v_exp_f32_e32 v12, v12
	s_nop 0
	v_add_f32_e32 v12, 1.0, v12
	v_rcp_f32_e32 v12, v12
	v_mul_f32_e32 v13, 0xbfb8aa3b, v5
	v_exp_f32_e32 v13, v13
	v_cvt_pk_bf16_f32 v12, v2, v12
	s_nop 0
	v_add_f32_e32 v13, 1.0, v13
	v_rcp_f32_e32 v15, v13
	v_mul_f32_e32 v13, 0xbfb8aa3b, v10
	v_exp_f32_e32 v13, v13
	s_nop 0
	v_add_f32_e32 v13, 1.0, v13
	v_rcp_f32_e32 v13, v13
	v_mul_f32_e32 v16, 0xbfb8aa3b, v6
	v_exp_f32_e32 v16, v16
	s_nop 0
	v_add_f32_e32 v16, 1.0, v16
	v_rcp_f32_e32 v16, v16
	v_mul_f32_e32 v17, 0xbfb8aa3b, v11
	v_exp_f32_e32 v17, v17
	s_nop 0
	v_add_f32_e32 v17, 1.0, v17
	v_rcp_f32_e32 v17, v17
	v_mul_f32_e32 v18, 0xbfb8aa3b, v7
	v_exp_f32_e32 v18, v18
	v_cvt_pk_bf16_f32 v13, v13, v17
	v_cvt_pk_bf16_f32 v14, v14, v15
	s_nop 0
	v_add_f32_e32 v18, 1.0, v18
	s_or_b32 s0, s76, 4
	s_ashr_i32 s1, s0, 31
	s_lshl_b64 s[0:1], s[0:1], 10
	v_rcp_f32_e32 v18, v18
	s_nop 0
	v_cvt_pk_bf16_f32 v15, v16, v18
	v_lshl_add_u64 v[16:17], v[148:149], 0, s[0:1]
	global_store_dwordx4 v[16:17], v[12:15], off nt

.LBB0_843:
	s_andn2_b64 vcc, exec, s[6:7]
	s_cbranch_vccnz .LBB0_845
	v_mul_f32_e32 v2, 0xbfb8aa3b, v128
	v_exp_f32_e32 v2, v2
	s_ashr_i32 s75, s74, 31
	v_add_f32_e32 v2, 1.0, v2
	v_rcp_f32_e32 v2, v2
	v_mul_f32_e32 v132, 0xbfb8aa3b, v124
	v_exp_f32_e32 v132, v132
	s_nop 0
	v_add_f32_e32 v132, 1.0, v132
	v_rcp_f32_e32 v134, v132
	v_mul_f32_e32 v132, 0xbfb8aa3b, v129
	v_exp_f32_e32 v132, v132
	s_nop 0
	v_add_f32_e32 v132, 1.0, v132
	v_rcp_f32_e32 v132, v132
	v_mul_f32_e32 v133, 0xbfb8aa3b, v125
	v_exp_f32_e32 v133, v133
	v_cvt_pk_bf16_f32 v132, v2, v132
	s_nop 0
	v_add_f32_e32 v133, 1.0, v133
	v_rcp_f32_e32 v135, v133
	v_mul_f32_e32 v133, 0xbfb8aa3b, v130
	v_exp_f32_e32 v133, v133
	s_nop 0
	v_add_f32_e32 v133, 1.0, v133
	v_rcp_f32_e32 v133, v133
	v_mul_f32_e32 v136, 0xbfb8aa3b, v126
	v_exp_f32_e32 v136, v136
	s_nop 0
	v_add_f32_e32 v136, 1.0, v136
	v_rcp_f32_e32 v136, v136
	v_mul_f32_e32 v137, 0xbfb8aa3b, v131
	v_exp_f32_e32 v137, v137
	s_nop 0
	v_add_f32_e32 v137, 1.0, v137
	v_rcp_f32_e32 v137, v137
	v_mul_f32_e32 v138, 0xbfb8aa3b, v127
	v_exp_f32_e32 v138, v138
	v_cvt_pk_bf16_f32 v133, v133, v137
	v_cvt_pk_bf16_f32 v134, v134, v135
	s_nop 0
	v_add_f32_e32 v138, 1.0, v138
	s_lshl_b64 s[6:7], s[74:75], 10
	v_rcp_f32_e32 v138, v138
	s_nop 0
	v_cvt_pk_bf16_f32 v135, v136, v138
	v_lshl_add_u64 v[136:137], v[148:149], 0, s[6:7]
	global_store_dwordx4 v[136:137], v[132:135], off nt

.LBB0_855:
	v_cndmask_b32_e64 v2, 0, 1, s[0:1]
	v_cmp_ne_u32_e64 s[42:43], 1, v2
	v_cndmask_b32_e64 v2, 0, 1, s[2:3]
	v_or_b32_e32 v132, s44, v164
	s_mov_b64 s[4:5], -1
	s_andn2_b64 vcc, exec, s[0:1]
	v_cmp_ne_u32_e64 s[40:41], 1, v2
	s_cbranch_vccnz .LBB0_863
	s_and_b64 vcc, exec, s[40:41]
	s_mov_b64 s[0:1], -1
	s_cbranch_vccnz .LBB0_860
	s_andn2_b64 vcc, exec, s[36:37]
	s_cbranch_vccnz .LBB0_859
	v_mul_f32_e32 v2, 0xbfb8aa3b, v120
	v_exp_f32_e32 v2, v2
	s_nop 0
	v_add_f32_e32 v2, 1.0, v2
	v_rcp_f32_e32 v2, v2
	v_mul_f32_e32 v124, 0xbfb8aa3b, v116
	v_exp_f32_e32 v124, v124
	s_nop 0
	v_add_f32_e32 v124, 1.0, v124
	v_rcp_f32_e32 v126, v124
	v_mul_f32_e32 v124, 0xbfb8aa3b, v121
	v_exp_f32_e32 v124, v124
	s_nop 0
	v_add_f32_e32 v124, 1.0, v124
	v_rcp_f32_e32 v124, v124
	v_mul_f32_e32 v125, 0xbfb8aa3b, v117
	v_exp_f32_e32 v125, v125
	v_cvt_pk_bf16_f32 v124, v2, v124
	s_nop 0
	v_add_f32_e32 v125, 1.0, v125
	v_rcp_f32_e32 v127, v125
	v_mul_f32_e32 v125, 0xbfb8aa3b, v122
	v_exp_f32_e32 v125, v125
	s_nop 0
	v_add_f32_e32 v125, 1.0, v125
	v_rcp_f32_e32 v125, v125
	v_mul_f32_e32 v128, 0xbfb8aa3b, v118
	v_exp_f32_e32 v128, v128
	s_nop 0
	v_add_f32_e32 v128, 1.0, v128
	v_rcp_f32_e32 v128, v128
	v_mul_f32_e32 v129, 0xbfb8aa3b, v123
	v_exp_f32_e32 v129, v129
	s_nop 0
	v_add_f32_e32 v129, 1.0, v129
	v_rcp_f32_e32 v129, v129
	v_mul_f32_e32 v130, 0xbfb8aa3b, v119
	v_exp_f32_e32 v130, v130
	v_cvt_pk_bf16_f32 v125, v125, v129
	v_cvt_pk_bf16_f32 v126, v126, v127
	s_nop 0
	v_add_f32_e32 v130, 1.0, v130
	s_or_b32 s0, s74, 4
	s_ashr_i32 s1, s0, 31
	s_lshl_b64 s[0:1], s[0:1], 10
	v_rcp_f32_e32 v130, v130
	s_nop 0
	v_cvt_pk_bf16_f32 v127, v128, v130
	v_lshl_add_u64 v[128:129], v[148:149], 0, s[0:1]
	global_store_dwordx4 v[128:129], v[124:127], off nt

.LBB0_879:
	s_andn2_b64 vcc, exec, s[0:1]
	s_cbranch_vccnz .LBB0_881
	v_mul_f32_e32 v2, 0xbfb8aa3b, v112
	v_exp_f32_e32 v2, v2
	s_ashr_i32 s77, s76, 31
	v_add_f32_e32 v2, 1.0, v2
	v_rcp_f32_e32 v2, v2
	v_mul_f32_e32 v116, 0xbfb8aa3b, v108
	v_exp_f32_e32 v116, v116
	s_nop 0
	v_add_f32_e32 v116, 1.0, v116
	v_rcp_f32_e32 v118, v116
	v_mul_f32_e32 v116, 0xbfb8aa3b, v113
	v_exp_f32_e32 v116, v116
	s_nop 0
	v_add_f32_e32 v116, 1.0, v116
	v_rcp_f32_e32 v116, v116
	v_mul_f32_e32 v117, 0xbfb8aa3b, v109
	v_exp_f32_e32 v117, v117
	v_cvt_pk_bf16_f32 v116, v2, v116
	s_nop 0
	v_add_f32_e32 v117, 1.0, v117
	v_rcp_f32_e32 v119, v117
	v_mul_f32_e32 v117, 0xbfb8aa3b, v114
	v_exp_f32_e32 v117, v117
	s_nop 0
	v_add_f32_e32 v117, 1.0, v117
	v_rcp_f32_e32 v117, v117
	v_mul_f32_e32 v121, 0xbfb8aa3b, v110
	v_exp_f32_e32 v121, v121
	s_nop 0
	v_add_f32_e32 v121, 1.0, v121
	v_rcp_f32_e32 v121, v121
	v_mul_f32_e32 v122, 0xbfb8aa3b, v115
	v_exp_f32_e32 v122, v122
	s_nop 0
	v_add_f32_e32 v122, 1.0, v122
	v_rcp_f32_e32 v122, v122
	v_mul_f32_e32 v123, 0xbfb8aa3b, v111
	v_exp_f32_e32 v123, v123
	v_cvt_pk_bf16_f32 v117, v117, v122
	v_cvt_pk_bf16_f32 v118, v118, v119
	s_nop 0
	v_add_f32_e32 v123, 1.0, v123
	s_lshl_b64 s[0:1], s[76:77], 10
	s_movk_i32 s77, 0x6000
	v_rcp_f32_e32 v123, v123
	s_nop 0
	v_cvt_pk_bf16_f32 v119, v121, v123
	v_lshl_add_u64 v[122:123], v[148:149], 0, s[0:1]
	global_store_dwordx4 v[122:123], v[116:119], off nt

.LBB0_890:
	s_and_b64 vcc, exec, s[40:41]
	s_cbranch_vccnz .LBB0_894
	s_andn2_b64 vcc, exec, s[36:37]
	s_cbranch_vccnz .LBB0_893
	v_mul_f32_e32 v2, 0xbfb8aa3b, v104
	v_exp_f32_e32 v2, v2
	s_nop 0
	v_add_f32_e32 v2, 1.0, v2
	v_rcp_f32_e32 v2, v2
	v_mul_f32_e32 v108, 0xbfb8aa3b, v100
	v_exp_f32_e32 v108, v108
	s_nop 0
	v_add_f32_e32 v108, 1.0, v108
	v_rcp_f32_e32 v110, v108
	v_mul_f32_e32 v108, 0xbfb8aa3b, v105
	v_exp_f32_e32 v108, v108
	s_nop 0
	v_add_f32_e32 v108, 1.0, v108
	v_rcp_f32_e32 v108, v108
	v_mul_f32_e32 v109, 0xbfb8aa3b, v101
	v_exp_f32_e32 v109, v109
	v_cvt_pk_bf16_f32 v108, v2, v108
	s_nop 0
	v_add_f32_e32 v109, 1.0, v109
	v_rcp_f32_e32 v111, v109
	v_mul_f32_e32 v109, 0xbfb8aa3b, v106
	v_exp_f32_e32 v109, v109
	s_nop 0
	v_add_f32_e32 v109, 1.0, v109
	v_rcp_f32_e32 v109, v109
	v_mul_f32_e32 v112, 0xbfb8aa3b, v102
	v_exp_f32_e32 v112, v112
	s_nop 0
	v_add_f32_e32 v112, 1.0, v112
	v_rcp_f32_e32 v112, v112
	v_mul_f32_e32 v113, 0xbfb8aa3b, v107
	v_exp_f32_e32 v113, v113
	s_nop 0
	v_add_f32_e32 v113, 1.0, v113
	v_rcp_f32_e32 v113, v113
	v_mul_f32_e32 v114, 0xbfb8aa3b, v103
	v_exp_f32_e32 v114, v114
	v_cvt_pk_bf16_f32 v109, v109, v113
	v_cvt_pk_bf16_f32 v110, v110, v111
	s_nop 0
	v_add_f32_e32 v114, 1.0, v114
	s_or_b32 s0, s76, 4
	s_ashr_i32 s1, s0, 31
	s_lshl_b64 s[0:1], s[0:1], 10
	v_rcp_f32_e32 v114, v114
	s_nop 0
	v_cvt_pk_bf16_f32 v111, v112, v114
	v_lshl_add_u64 v[112:113], v[148:149], 0, s[0:1]
	global_store_dwordx4 v[112:113], v[108:111], off nt

.LBB0_911:
	s_andn2_b64 vcc, exec, s[0:1]
	s_cbranch_vccnz .LBB0_913
	v_mul_f32_e32 v2, 0xbfb8aa3b, v96
	v_exp_f32_e32 v2, v2
	s_ashr_i32 s77, s76, 31
	v_add_f32_e32 v2, 1.0, v2
	v_rcp_f32_e32 v2, v2
	v_mul_f32_e32 v100, 0xbfb8aa3b, v92
	v_exp_f32_e32 v100, v100
	s_nop 0
	v_add_f32_e32 v100, 1.0, v100
	v_rcp_f32_e32 v102, v100
	v_mul_f32_e32 v100, 0xbfb8aa3b, v97
	v_exp_f32_e32 v100, v100
	s_nop 0
	v_add_f32_e32 v100, 1.0, v100
	v_rcp_f32_e32 v100, v100
	v_mul_f32_e32 v101, 0xbfb8aa3b, v93
	v_exp_f32_e32 v101, v101
	v_cvt_pk_bf16_f32 v100, v2, v100
	s_nop 0
	v_add_f32_e32 v101, 1.0, v101
	v_rcp_f32_e32 v103, v101
	v_mul_f32_e32 v101, 0xbfb8aa3b, v98
	v_exp_f32_e32 v101, v101
	s_nop 0
	v_add_f32_e32 v101, 1.0, v101
	v_rcp_f32_e32 v101, v101
	v_mul_f32_e32 v105, 0xbfb8aa3b, v94
	v_exp_f32_e32 v105, v105
	s_nop 0
	v_add_f32_e32 v105, 1.0, v105
	v_rcp_f32_e32 v105, v105
	v_mul_f32_e32 v106, 0xbfb8aa3b, v99
	v_exp_f32_e32 v106, v106
	s_nop 0
	v_add_f32_e32 v106, 1.0, v106
	v_rcp_f32_e32 v106, v106
	v_mul_f32_e32 v107, 0xbfb8aa3b, v95
	v_exp_f32_e32 v107, v107
	v_cvt_pk_bf16_f32 v101, v101, v106
	v_cvt_pk_bf16_f32 v102, v102, v103
	s_nop 0
	v_add_f32_e32 v107, 1.0, v107
	s_lshl_b64 s[0:1], s[76:77], 10
	s_movk_i32 s77, 0x6000
	v_rcp_f32_e32 v107, v107
	s_nop 0
	v_cvt_pk_bf16_f32 v103, v105, v107
	v_lshl_add_u64 v[106:107], v[148:149], 0, s[0:1]
	global_store_dwordx4 v[106:107], v[100:103], off nt

.LBB0_922:
	s_and_b64 vcc, exec, s[40:41]
	s_cbranch_vccnz .LBB0_926
	s_andn2_b64 vcc, exec, s[36:37]
	s_cbranch_vccnz .LBB0_925
	v_mul_f32_e32 v2, 0xbfb8aa3b, v88
	v_exp_f32_e32 v2, v2
	s_nop 0
	v_add_f32_e32 v2, 1.0, v2
	v_rcp_f32_e32 v2, v2
	v_mul_f32_e32 v92, 0xbfb8aa3b, v84
	v_exp_f32_e32 v92, v92
	s_nop 0
	v_add_f32_e32 v92, 1.0, v92
	v_rcp_f32_e32 v94, v92
	v_mul_f32_e32 v92, 0xbfb8aa3b, v89
	v_exp_f32_e32 v92, v92
	s_nop 0
	v_add_f32_e32 v92, 1.0, v92
	v_rcp_f32_e32 v92, v92
	v_mul_f32_e32 v93, 0xbfb8aa3b, v85
	v_exp_f32_e32 v93, v93
	v_cvt_pk_bf16_f32 v92, v2, v92
	s_nop 0
	v_add_f32_e32 v93, 1.0, v93
	v_rcp_f32_e32 v95, v93
	v_mul_f32_e32 v93, 0xbfb8aa3b, v90
	v_exp_f32_e32 v93, v93
	s_nop 0
	v_add_f32_e32 v93, 1.0, v93
	v_rcp_f32_e32 v93, v93
	v_mul_f32_e32 v96, 0xbfb8aa3b, v86
	v_exp_f32_e32 v96, v96
	s_nop 0
	v_add_f32_e32 v96, 1.0, v96
	v_rcp_f32_e32 v96, v96
	v_mul_f32_e32 v97, 0xbfb8aa3b, v91
	v_exp_f32_e32 v97, v97
	s_nop 0
	v_add_f32_e32 v97, 1.0, v97
	v_rcp_f32_e32 v97, v97
	v_mul_f32_e32 v98, 0xbfb8aa3b, v87
	v_exp_f32_e32 v98, v98
	v_cvt_pk_bf16_f32 v93, v93, v97
	v_cvt_pk_bf16_f32 v94, v94, v95
	s_nop 0
	v_add_f32_e32 v98, 1.0, v98
	s_or_b32 s0, s76, 4
	s_ashr_i32 s1, s0, 31
	s_lshl_b64 s[0:1], s[0:1], 10
	v_rcp_f32_e32 v98, v98
	s_nop 0
	v_cvt_pk_bf16_f32 v95, v96, v98
	v_lshl_add_u64 v[96:97], v[148:149], 0, s[0:1]
	global_store_dwordx4 v[96:97], v[92:95], off nt

.LBB0_943:
	s_andn2_b64 vcc, exec, s[0:1]
	s_cbranch_vccnz .LBB0_945
	v_mul_f32_e32 v2, 0xbfb8aa3b, v80
	v_exp_f32_e32 v2, v2
	s_ashr_i32 s77, s76, 31
	v_add_f32_e32 v2, 1.0, v2
	v_rcp_f32_e32 v2, v2
	v_mul_f32_e32 v84, 0xbfb8aa3b, v76
	v_exp_f32_e32 v84, v84
	s_nop 0
	v_add_f32_e32 v84, 1.0, v84
	v_rcp_f32_e32 v86, v84
	v_mul_f32_e32 v84, 0xbfb8aa3b, v81
	v_exp_f32_e32 v84, v84
	s_nop 0
	v_add_f32_e32 v84, 1.0, v84
	v_rcp_f32_e32 v84, v84
	v_mul_f32_e32 v85, 0xbfb8aa3b, v77
	v_exp_f32_e32 v85, v85
	v_cvt_pk_bf16_f32 v84, v2, v84
	s_nop 0
	v_add_f32_e32 v85, 1.0, v85
	v_rcp_f32_e32 v87, v85
	v_mul_f32_e32 v85, 0xbfb8aa3b, v82
	v_exp_f32_e32 v85, v85
	s_nop 0
	v_add_f32_e32 v85, 1.0, v85
	v_rcp_f32_e32 v85, v85
	v_mul_f32_e32 v89, 0xbfb8aa3b, v78
	v_exp_f32_e32 v89, v89
	s_nop 0
	v_add_f32_e32 v89, 1.0, v89
	v_rcp_f32_e32 v89, v89
	v_mul_f32_e32 v90, 0xbfb8aa3b, v83
	v_exp_f32_e32 v90, v90
	s_nop 0
	v_add_f32_e32 v90, 1.0, v90
	v_rcp_f32_e32 v90, v90
	v_mul_f32_e32 v91, 0xbfb8aa3b, v79
	v_exp_f32_e32 v91, v91
	v_cvt_pk_bf16_f32 v85, v85, v90
	v_cvt_pk_bf16_f32 v86, v86, v87
	s_nop 0
	v_add_f32_e32 v91, 1.0, v91
	s_lshl_b64 s[0:1], s[76:77], 10
	s_movk_i32 s77, 0x6000
	v_rcp_f32_e32 v91, v91
	s_nop 0
	v_cvt_pk_bf16_f32 v87, v89, v91
	v_lshl_add_u64 v[90:91], v[148:149], 0, s[0:1]
	global_store_dwordx4 v[90:91], v[84:87], off nt

.LBB0_954:
	s_and_b64 vcc, exec, s[40:41]
	s_cbranch_vccnz .LBB0_958
	s_andn2_b64 vcc, exec, s[36:37]
	s_cbranch_vccnz .LBB0_957
	v_mul_f32_e32 v2, 0xbfb8aa3b, v72
	v_exp_f32_e32 v2, v2
	s_nop 0
	v_add_f32_e32 v2, 1.0, v2
	v_rcp_f32_e32 v2, v2
	v_mul_f32_e32 v76, 0xbfb8aa3b, v68
	v_exp_f32_e32 v76, v76
	s_nop 0
	v_add_f32_e32 v76, 1.0, v76
	v_rcp_f32_e32 v78, v76
	v_mul_f32_e32 v76, 0xbfb8aa3b, v73
	v_exp_f32_e32 v76, v76
	s_nop 0
	v_add_f32_e32 v76, 1.0, v76
	v_rcp_f32_e32 v76, v76
	v_mul_f32_e32 v77, 0xbfb8aa3b, v69
	v_exp_f32_e32 v77, v77
	v_cvt_pk_bf16_f32 v76, v2, v76
	s_nop 0
	v_add_f32_e32 v77, 1.0, v77
	v_rcp_f32_e32 v79, v77
	v_mul_f32_e32 v77, 0xbfb8aa3b, v74
	v_exp_f32_e32 v77, v77
	s_nop 0
	v_add_f32_e32 v77, 1.0, v77
	v_rcp_f32_e32 v77, v77
	v_mul_f32_e32 v80, 0xbfb8aa3b, v70
	v_exp_f32_e32 v80, v80
	s_nop 0
	v_add_f32_e32 v80, 1.0, v80
	v_rcp_f32_e32 v80, v80
	v_mul_f32_e32 v81, 0xbfb8aa3b, v75
	v_exp_f32_e32 v81, v81
	s_nop 0
	v_add_f32_e32 v81, 1.0, v81
	v_rcp_f32_e32 v81, v81
	v_mul_f32_e32 v82, 0xbfb8aa3b, v71
	v_exp_f32_e32 v82, v82
	v_cvt_pk_bf16_f32 v77, v77, v81
	v_cvt_pk_bf16_f32 v78, v78, v79
	s_nop 0
	v_add_f32_e32 v82, 1.0, v82
	s_or_b32 s0, s76, 4
	s_ashr_i32 s1, s0, 31
	s_lshl_b64 s[0:1], s[0:1], 10
	v_rcp_f32_e32 v82, v82
	s_nop 0
	v_cvt_pk_bf16_f32 v79, v80, v82
	v_lshl_add_u64 v[80:81], v[148:149], 0, s[0:1]
	global_store_dwordx4 v[80:81], v[76:79], off nt

.LBB0_972:
	s_andn2_b64 vcc, exec, s[0:1]
	s_cbranch_vccnz .LBB0_974
	v_mul_f32_e32 v2, 0xbfb8aa3b, v64
	v_exp_f32_e32 v2, v2
	s_ashr_i32 s77, s76, 31
	v_add_f32_e32 v2, 1.0, v2
	v_rcp_f32_e32 v2, v2
	v_mul_f32_e32 v68, 0xbfb8aa3b, v60
	v_exp_f32_e32 v68, v68
	s_nop 0
	v_add_f32_e32 v68, 1.0, v68
	v_rcp_f32_e32 v70, v68
	v_mul_f32_e32 v68, 0xbfb8aa3b, v65
	v_exp_f32_e32 v68, v68
	s_nop 0
	v_add_f32_e32 v68, 1.0, v68
	v_rcp_f32_e32 v68, v68
	v_mul_f32_e32 v69, 0xbfb8aa3b, v61
	v_exp_f32_e32 v69, v69
	v_cvt_pk_bf16_f32 v68, v2, v68
	s_nop 0
	v_add_f32_e32 v69, 1.0, v69
	v_rcp_f32_e32 v71, v69
	v_mul_f32_e32 v69, 0xbfb8aa3b, v66
	v_exp_f32_e32 v69, v69
	s_nop 0
	v_add_f32_e32 v69, 1.0, v69
	v_rcp_f32_e32 v69, v69
	v_mul_f32_e32 v72, 0xbfb8aa3b, v62
	v_exp_f32_e32 v72, v72
	s_nop 0
	v_add_f32_e32 v72, 1.0, v72
	v_rcp_f32_e32 v72, v72
	v_mul_f32_e32 v73, 0xbfb8aa3b, v67
	v_exp_f32_e32 v73, v73
	s_nop 0
	v_add_f32_e32 v73, 1.0, v73
	v_rcp_f32_e32 v73, v73
	v_mul_f32_e32 v74, 0xbfb8aa3b, v63
	v_exp_f32_e32 v74, v74
	v_cvt_pk_bf16_f32 v69, v69, v73
	v_cvt_pk_bf16_f32 v70, v70, v71
	s_nop 0
	v_add_f32_e32 v74, 1.0, v74
	s_lshl_b64 s[0:1], s[76:77], 10
	s_movk_i32 s77, 0x6000
	v_rcp_f32_e32 v74, v74
	s_nop 0
	v_cvt_pk_bf16_f32 v71, v72, v74
	v_lshl_add_u64 v[72:73], v[148:149], 0, s[0:1]
	global_store_dwordx4 v[72:73], v[68:71], off nt

.LBB0_986:
	s_and_b64 vcc, exec, s[40:41]
	s_cbranch_vccnz .LBB0_990
	s_andn2_b64 vcc, exec, s[36:37]
	s_cbranch_vccnz .LBB0_989
	v_mul_f32_e32 v2, 0xbfb8aa3b, v56
	v_exp_f32_e32 v2, v2
	s_nop 0
	v_add_f32_e32 v2, 1.0, v2
	v_rcp_f32_e32 v2, v2
	v_mul_f32_e32 v60, 0xbfb8aa3b, v52
	v_exp_f32_e32 v60, v60
	s_nop 0
	v_add_f32_e32 v60, 1.0, v60
	v_rcp_f32_e32 v62, v60
	v_mul_f32_e32 v60, 0xbfb8aa3b, v57
	v_exp_f32_e32 v60, v60
	s_nop 0
	v_add_f32_e32 v60, 1.0, v60
	v_rcp_f32_e32 v60, v60
	v_mul_f32_e32 v61, 0xbfb8aa3b, v53
	v_exp_f32_e32 v61, v61
	v_cvt_pk_bf16_f32 v60, v2, v60
	s_nop 0
	v_add_f32_e32 v61, 1.0, v61
	v_rcp_f32_e32 v63, v61
	v_mul_f32_e32 v61, 0xbfb8aa3b, v58
	v_exp_f32_e32 v61, v61
	s_nop 0
	v_add_f32_e32 v61, 1.0, v61
	v_rcp_f32_e32 v61, v61
	v_mul_f32_e32 v64, 0xbfb8aa3b, v54
	v_exp_f32_e32 v64, v64
	s_nop 0
	v_add_f32_e32 v64, 1.0, v64
	v_rcp_f32_e32 v64, v64
	v_mul_f32_e32 v65, 0xbfb8aa3b, v59
	v_exp_f32_e32 v65, v65
	s_nop 0
	v_add_f32_e32 v65, 1.0, v65
	v_rcp_f32_e32 v65, v65
	v_mul_f32_e32 v66, 0xbfb8aa3b, v55
	v_exp_f32_e32 v66, v66
	v_cvt_pk_bf16_f32 v61, v61, v65
	v_cvt_pk_bf16_f32 v62, v62, v63
	s_nop 0
	v_add_f32_e32 v66, 1.0, v66
	s_or_b32 s0, s76, 4
	s_ashr_i32 s1, s0, 31
	s_lshl_b64 s[0:1], s[0:1], 10
	v_rcp_f32_e32 v66, v66
	s_nop 0
	v_cvt_pk_bf16_f32 v63, v64, v66
	v_lshl_add_u64 v[64:65], v[148:149], 0, s[0:1]
	global_store_dwordx4 v[64:65], v[60:63], off nt

.LBB0_1007:
	s_andn2_b64 vcc, exec, s[0:1]
	s_cbranch_vccnz .LBB0_1009
	v_mul_f32_e32 v2, 0xbfb8aa3b, v48
	v_exp_f32_e32 v2, v2
	s_ashr_i32 s77, s76, 31
	v_add_f32_e32 v2, 1.0, v2
	v_rcp_f32_e32 v2, v2
	v_mul_f32_e32 v52, 0xbfb8aa3b, v44
	v_exp_f32_e32 v52, v52
	s_nop 0
	v_add_f32_e32 v52, 1.0, v52
	v_rcp_f32_e32 v54, v52
	v_mul_f32_e32 v52, 0xbfb8aa3b, v49
	v_exp_f32_e32 v52, v52
	s_nop 0
	v_add_f32_e32 v52, 1.0, v52
	v_rcp_f32_e32 v52, v52
	v_mul_f32_e32 v53, 0xbfb8aa3b, v45
	v_exp_f32_e32 v53, v53
	v_cvt_pk_bf16_f32 v52, v2, v52
	s_nop 0
	v_add_f32_e32 v53, 1.0, v53
	v_rcp_f32_e32 v55, v53
	v_mul_f32_e32 v53, 0xbfb8aa3b, v50
	v_exp_f32_e32 v53, v53
	s_nop 0
	v_add_f32_e32 v53, 1.0, v53
	v_rcp_f32_e32 v53, v53
	v_mul_f32_e32 v57, 0xbfb8aa3b, v46
	v_exp_f32_e32 v57, v57
	s_nop 0
	v_add_f32_e32 v57, 1.0, v57
	v_rcp_f32_e32 v57, v57
	v_mul_f32_e32 v58, 0xbfb8aa3b, v51
	v_exp_f32_e32 v58, v58
	s_nop 0
	v_add_f32_e32 v58, 1.0, v58
	v_rcp_f32_e32 v58, v58
	v_mul_f32_e32 v59, 0xbfb8aa3b, v47
	v_exp_f32_e32 v59, v59
	v_cvt_pk_bf16_f32 v53, v53, v58
	v_cvt_pk_bf16_f32 v54, v54, v55
	s_nop 0
	v_add_f32_e32 v59, 1.0, v59
	s_lshl_b64 s[0:1], s[76:77], 10
	s_movk_i32 s77, 0x6000
	v_rcp_f32_e32 v59, v59
	s_nop 0
	v_cvt_pk_bf16_f32 v55, v57, v59
	v_lshl_add_u64 v[58:59], v[148:149], 0, s[0:1]
	global_store_dwordx4 v[58:59], v[52:55], off nt

.LBB0_1018:
	s_and_b64 vcc, exec, s[40:41]
	s_cbranch_vccnz .LBB0_1022
	s_andn2_b64 vcc, exec, s[36:37]
	s_cbranch_vccnz .LBB0_1021
	v_mul_f32_e32 v2, 0xbfb8aa3b, v40
	v_exp_f32_e32 v2, v2
	s_nop 0
	v_add_f32_e32 v2, 1.0, v2
	v_rcp_f32_e32 v2, v2
	v_mul_f32_e32 v44, 0xbfb8aa3b, v36
	v_exp_f32_e32 v44, v44
	s_nop 0
	v_add_f32_e32 v44, 1.0, v44
	v_rcp_f32_e32 v46, v44
	v_mul_f32_e32 v44, 0xbfb8aa3b, v41
	v_exp_f32_e32 v44, v44
	s_nop 0
	v_add_f32_e32 v44, 1.0, v44
	v_rcp_f32_e32 v44, v44
	v_mul_f32_e32 v45, 0xbfb8aa3b, v37
	v_exp_f32_e32 v45, v45
	v_cvt_pk_bf16_f32 v44, v2, v44
	s_nop 0
	v_add_f32_e32 v45, 1.0, v45
	v_rcp_f32_e32 v47, v45
	v_mul_f32_e32 v45, 0xbfb8aa3b, v42
	v_exp_f32_e32 v45, v45
	s_nop 0
	v_add_f32_e32 v45, 1.0, v45
	v_rcp_f32_e32 v45, v45
	v_mul_f32_e32 v48, 0xbfb8aa3b, v38
	v_exp_f32_e32 v48, v48
	s_nop 0
	v_add_f32_e32 v48, 1.0, v48
	v_rcp_f32_e32 v48, v48
	v_mul_f32_e32 v49, 0xbfb8aa3b, v43
	v_exp_f32_e32 v49, v49
	s_nop 0
	v_add_f32_e32 v49, 1.0, v49
	v_rcp_f32_e32 v49, v49
	v_mul_f32_e32 v50, 0xbfb8aa3b, v39
	v_exp_f32_e32 v50, v50
	v_cvt_pk_bf16_f32 v45, v45, v49
	v_cvt_pk_bf16_f32 v46, v46, v47
	s_nop 0
	v_add_f32_e32 v50, 1.0, v50
	s_or_b32 s0, s76, 4
	s_ashr_i32 s1, s0, 31
	s_lshl_b64 s[0:1], s[0:1], 10
	v_rcp_f32_e32 v50, v50
	s_nop 0
	v_cvt_pk_bf16_f32 v47, v48, v50
	v_lshl_add_u64 v[48:49], v[148:149], 0, s[0:1]
	global_store_dwordx4 v[48:49], v[44:47], off nt

.LBB0_1039:
	s_andn2_b64 vcc, exec, s[0:1]
	s_cbranch_vccnz .LBB0_1041
	v_mul_f32_e32 v2, 0xbfb8aa3b, v32
	v_exp_f32_e32 v2, v2
	s_ashr_i32 s77, s76, 31
	v_add_f32_e32 v2, 1.0, v2
	v_rcp_f32_e32 v2, v2
	v_mul_f32_e32 v36, 0xbfb8aa3b, v28
	v_exp_f32_e32 v36, v36
	s_nop 0
	v_add_f32_e32 v36, 1.0, v36
	v_rcp_f32_e32 v38, v36
	v_mul_f32_e32 v36, 0xbfb8aa3b, v33
	v_exp_f32_e32 v36, v36
	s_nop 0
	v_add_f32_e32 v36, 1.0, v36
	v_rcp_f32_e32 v36, v36
	v_mul_f32_e32 v37, 0xbfb8aa3b, v29
	v_exp_f32_e32 v37, v37
	v_cvt_pk_bf16_f32 v36, v2, v36
	s_nop 0
	v_add_f32_e32 v37, 1.0, v37
	v_rcp_f32_e32 v39, v37
	v_mul_f32_e32 v37, 0xbfb8aa3b, v34
	v_exp_f32_e32 v37, v37
	s_nop 0
	v_add_f32_e32 v37, 1.0, v37
	v_rcp_f32_e32 v37, v37
	v_mul_f32_e32 v41, 0xbfb8aa3b, v30
	v_exp_f32_e32 v41, v41
	s_nop 0
	v_add_f32_e32 v41, 1.0, v41
	v_rcp_f32_e32 v41, v41
	v_mul_f32_e32 v42, 0xbfb8aa3b, v35
	v_exp_f32_e32 v42, v42
	s_nop 0
	v_add_f32_e32 v42, 1.0, v42
	v_rcp_f32_e32 v42, v42
	v_mul_f32_e32 v43, 0xbfb8aa3b, v31
	v_exp_f32_e32 v43, v43
	v_cvt_pk_bf16_f32 v37, v37, v42
	v_cvt_pk_bf16_f32 v38, v38, v39
	s_nop 0
	v_add_f32_e32 v43, 1.0, v43
	s_lshl_b64 s[0:1], s[76:77], 10
	s_movk_i32 s77, 0x6000
	v_rcp_f32_e32 v43, v43
	s_nop 0
	v_cvt_pk_bf16_f32 v39, v41, v43
	v_lshl_add_u64 v[42:43], v[148:149], 0, s[0:1]
	global_store_dwordx4 v[42:43], v[36:39], off nt

.LBB0_1050:
	s_and_b64 vcc, exec, s[40:41]
	s_cbranch_vccnz .LBB0_1054
	s_andn2_b64 vcc, exec, s[36:37]
	s_cbranch_vccnz .LBB0_1053
	v_mul_f32_e32 v2, 0xbfb8aa3b, v24
	v_exp_f32_e32 v2, v2
	s_nop 0
	v_add_f32_e32 v2, 1.0, v2
	v_rcp_f32_e32 v2, v2
	v_mul_f32_e32 v28, 0xbfb8aa3b, v20
	v_exp_f32_e32 v28, v28
	s_nop 0
	v_add_f32_e32 v28, 1.0, v28
	v_rcp_f32_e32 v30, v28
	v_mul_f32_e32 v28, 0xbfb8aa3b, v25
	v_exp_f32_e32 v28, v28
	s_nop 0
	v_add_f32_e32 v28, 1.0, v28
	v_rcp_f32_e32 v28, v28
	v_mul_f32_e32 v29, 0xbfb8aa3b, v21
	v_exp_f32_e32 v29, v29
	v_cvt_pk_bf16_f32 v28, v2, v28
	s_nop 0
	v_add_f32_e32 v29, 1.0, v29
	v_rcp_f32_e32 v31, v29
	v_mul_f32_e32 v29, 0xbfb8aa3b, v26
	v_exp_f32_e32 v29, v29
	s_nop 0
	v_add_f32_e32 v29, 1.0, v29
	v_rcp_f32_e32 v29, v29
	v_mul_f32_e32 v32, 0xbfb8aa3b, v22
	v_exp_f32_e32 v32, v32
	s_nop 0
	v_add_f32_e32 v32, 1.0, v32
	v_rcp_f32_e32 v32, v32
	v_mul_f32_e32 v33, 0xbfb8aa3b, v27
	v_exp_f32_e32 v33, v33
	s_nop 0
	v_add_f32_e32 v33, 1.0, v33
	v_rcp_f32_e32 v33, v33
	v_mul_f32_e32 v34, 0xbfb8aa3b, v23
	v_exp_f32_e32 v34, v34
	v_cvt_pk_bf16_f32 v29, v29, v33
	v_cvt_pk_bf16_f32 v30, v30, v31
	s_nop 0
	v_add_f32_e32 v34, 1.0, v34
	s_or_b32 s0, s76, 4
	s_ashr_i32 s1, s0, 31
	s_lshl_b64 s[0:1], s[0:1], 10
	v_rcp_f32_e32 v34, v34
	s_nop 0
	v_cvt_pk_bf16_f32 v31, v32, v34
	v_lshl_add_u64 v[32:33], v[148:149], 0, s[0:1]
	global_store_dwordx4 v[32:33], v[28:31], off nt

.LBB0_1072:
	s_andn2_b64 vcc, exec, s[0:1]
	s_cbranch_vccnz .LBB0_1074
	v_mul_f32_e32 v2, 0xbfb8aa3b, v16
	v_exp_f32_e32 v2, v2
	s_ashr_i32 s75, s74, 31
	v_add_f32_e32 v2, 1.0, v2
	v_rcp_f32_e32 v2, v2
	v_mul_f32_e32 v20, 0xbfb8aa3b, v12
	v_exp_f32_e32 v20, v20
	s_nop 0
	v_add_f32_e32 v20, 1.0, v20
	v_rcp_f32_e32 v22, v20
	v_mul_f32_e32 v20, 0xbfb8aa3b, v17
	v_exp_f32_e32 v20, v20
	s_nop 0
	v_add_f32_e32 v20, 1.0, v20
	v_rcp_f32_e32 v20, v20
	v_mul_f32_e32 v21, 0xbfb8aa3b, v13
	v_exp_f32_e32 v21, v21
	v_cvt_pk_bf16_f32 v20, v2, v20
	s_nop 0
	v_add_f32_e32 v21, 1.0, v21
	v_rcp_f32_e32 v23, v21
	v_mul_f32_e32 v21, 0xbfb8aa3b, v18
	v_exp_f32_e32 v21, v21
	s_nop 0
	v_add_f32_e32 v21, 1.0, v21
	v_rcp_f32_e32 v21, v21
	v_mul_f32_e32 v25, 0xbfb8aa3b, v14
	v_exp_f32_e32 v25, v25
	s_nop 0
	v_add_f32_e32 v25, 1.0, v25
	v_rcp_f32_e32 v25, v25
	v_mul_f32_e32 v26, 0xbfb8aa3b, v19
	v_exp_f32_e32 v26, v26
	s_nop 0
	v_add_f32_e32 v26, 1.0, v26
	v_rcp_f32_e32 v26, v26
	v_mul_f32_e32 v27, 0xbfb8aa3b, v15
	v_exp_f32_e32 v27, v27
	v_cvt_pk_bf16_f32 v21, v21, v26
	v_cvt_pk_bf16_f32 v22, v22, v23
	s_nop 0
	v_add_f32_e32 v27, 1.0, v27
	s_lshl_b64 s[0:1], s[74:75], 10
	v_rcp_f32_e32 v27, v27
	s_nop 0
	v_cvt_pk_bf16_f32 v23, v25, v27
	v_lshl_add_u64 v[26:27], v[148:149], 0, s[0:1]
	global_store_dwordx4 v[26:27], v[20:23], off nt

.LBB0_1083:
	s_and_b64 vcc, exec, s[40:41]
	s_cbranch_vccnz .LBB0_1087
	s_andn2_b64 vcc, exec, s[36:37]
	s_cbranch_vccnz .LBB0_1086
	v_mul_f32_e32 v2, 0xbfb8aa3b, v8
	v_exp_f32_e32 v2, v2
	s_nop 0
	v_add_f32_e32 v2, 1.0, v2
	v_rcp_f32_e32 v2, v2
	v_mul_f32_e32 v12, 0xbfb8aa3b, v4
	v_exp_f32_e32 v12, v12
	s_nop 0
	v_add_f32_e32 v12, 1.0, v12
	v_rcp_f32_e32 v14, v12
	v_mul_f32_e32 v12, 0xbfb8aa3b, v9
	v_exp_f32_e32 v12, v12
	s_nop 0
	v_add_f32_e32 v12, 1.0, v12
	v_rcp_f32_e32 v12, v12
	v_mul_f32_e32 v13, 0xbfb8aa3b, v5
	v_exp_f32_e32 v13, v13
	v_cvt_pk_bf16_f32 v12, v2, v12
	s_nop 0
	v_add_f32_e32 v13, 1.0, v13
	v_rcp_f32_e32 v15, v13
	v_mul_f32_e32 v13, 0xbfb8aa3b, v10
	v_exp_f32_e32 v13, v13
	s_nop 0
	v_add_f32_e32 v13, 1.0, v13
	v_rcp_f32_e32 v13, v13
	v_mul_f32_e32 v16, 0xbfb8aa3b, v6
	v_exp_f32_e32 v16, v16
	s_nop 0
	v_add_f32_e32 v16, 1.0, v16
	v_rcp_f32_e32 v16, v16
	v_mul_f32_e32 v17, 0xbfb8aa3b, v11
	v_exp_f32_e32 v17, v17
	s_nop 0
	v_add_f32_e32 v17, 1.0, v17
	v_rcp_f32_e32 v17, v17
	v_mul_f32_e32 v18, 0xbfb8aa3b, v7
	v_exp_f32_e32 v18, v18
	v_cvt_pk_bf16_f32 v13, v13, v17
	v_cvt_pk_bf16_f32 v14, v14, v15
	s_nop 0
	v_add_f32_e32 v18, 1.0, v18
	s_or_b32 s0, s74, 4
	s_ashr_i32 s1, s0, 31
	s_lshl_b64 s[0:1], s[0:1], 10
	v_rcp_f32_e32 v18, v18
	s_nop 0
	v_cvt_pk_bf16_f32 v15, v16, v18
	v_lshl_add_u64 v[16:17], v[148:149], 0, s[0:1]
	global_store_dwordx4 v[16:17], v[12:15], off nt
